# attention: removed the vmcnt(3..0) over-drain ladder before the second-half K/V LDS writes (own drain on the last-iteration skip path)
# baseline (speedup 1.0000x reference)
.LBB0_1147:
	ds_read_b64_tr_b16 v[220:221], v198 offset:0
	ds_read_b64_tr_b16 v[222:223], v198 offset:0x800
	ds_read_b64_tr_b16 v[224:225], v198 offset:0x1000
	ds_read_b64_tr_b16 v[226:227], v198 offset:0x1800
	ds_read_b64_tr_b16 v[228:229], v198 offset:0x2000
	ds_read_b64_tr_b16 v[230:231], v198 offset:0x2800
	ds_read_b64_tr_b16 v[232:233], v198 offset:0x3000
	ds_read_b64_tr_b16 v[234:235], v198 offset:0x3800
	s_waitcnt lgkmcnt(0)
	s_nop 0
	v_mfma_f32_32x32x16_bf16 v[18:33], v[162:165], v[220:223], v[18:33]
	ds_read_b64_tr_b16 v[220:221], v198 offset:0x200
	ds_read_b64_tr_b16 v[222:223], v198 offset:0xa00
	v_mfma_f32_32x32x16_bf16 v[18:33], v[166:169], v[224:227], v[18:33]
	ds_read_b64_tr_b16 v[224:225], v198 offset:0x1200
	ds_read_b64_tr_b16 v[226:227], v198 offset:0x1a00
	v_mfma_f32_32x32x16_bf16 v[18:33], v[170:173], v[228:231], v[18:33]
	ds_read_b64_tr_b16 v[228:229], v198 offset:0x2200
	ds_read_b64_tr_b16 v[230:231], v198 offset:0x2a00
	ds_read_b64_tr_b16 v[236:237], v198 offset:0x3200
	ds_read_b64_tr_b16 v[238:239], v198 offset:0x3a00
	s_waitcnt lgkmcnt(0)
	v_mfma_f32_32x32x16_bf16 v[18:33], v[174:177], v[232:235], v[18:33]
	v_mfma_f32_32x32x16_bf16 v[50:65], v[162:165], v[220:223], v[50:65]
	ds_read_b64_tr_b16 v[220:221], v198 offset:0x400
	ds_read_b64_tr_b16 v[222:223], v198 offset:0xc00
	v_mfma_f32_32x32x16_bf16 v[50:65], v[166:169], v[224:227], v[50:65]
	ds_read_b64_tr_b16 v[224:225], v198 offset:0x1400
	ds_read_b64_tr_b16 v[226:227], v198 offset:0x1c00
	v_mfma_f32_32x32x16_bf16 v[50:65], v[170:173], v[228:231], v[50:65]
	ds_read_b64_tr_b16 v[228:229], v198 offset:0x2400
	ds_read_b64_tr_b16 v[230:231], v198 offset:0x2c00
	ds_read_b64_tr_b16 v[232:233], v198 offset:0x3400
	ds_read_b64_tr_b16 v[234:235], v198 offset:0x3c00
	s_waitcnt lgkmcnt(0)
	v_mfma_f32_32x32x16_bf16 v[50:65], v[174:177], v[236:239], v[50:65]
	v_mfma_f32_32x32x16_bf16 v[34:49], v[162:165], v[220:223], v[34:49]
	ds_read_b64_tr_b16 v[220:221], v198 offset:0x600
	ds_read_b64_tr_b16 v[222:223], v198 offset:0xe00
	v_mfma_f32_32x32x16_bf16 v[34:49], v[166:169], v[224:227], v[34:49]
	ds_read_b64_tr_b16 v[224:225], v198 offset:0x1600
	ds_read_b64_tr_b16 v[226:227], v198 offset:0x1e00
	v_mfma_f32_32x32x16_bf16 v[34:49], v[170:173], v[228:231], v[34:49]
	ds_read_b64_tr_b16 v[228:229], v198 offset:0x2600
	ds_read_b64_tr_b16 v[230:231], v198 offset:0x2e00
	ds_read_b64_tr_b16 v[236:237], v198 offset:0x3600
	ds_read_b64_tr_b16 v[238:239], v198 offset:0x3e00
	s_waitcnt lgkmcnt(0)
	v_mfma_f32_32x32x16_bf16 v[34:49], v[174:177], v[232:235], v[34:49]
	v_mfma_f32_32x32x16_bf16 v[2:17], v[162:165], v[220:223], v[2:17]
	v_max_f32_e32 v1, v83, v83
	v_max_f32_e32 v200, v82, v82
	v_max_f32_e32 v1, v200, v1
	v_max3_f32 v1, v1, v84, v85
	v_max3_f32 v1, v1, v86, v87
	v_max3_f32 v1, v1, v88, v89
	v_max3_f32 v1, v1, v90, v91
	v_max3_f32 v1, v1, v92, v93
	v_mfma_f32_32x32x16_bf16 v[2:17], v[166:169], v[224:227], v[2:17]
	v_max3_f32 v1, v1, v94, v95
	v_max3_f32 v1, v1, v96, v97
	v_max3_f32 v1, v1, v66, v67
	v_max3_f32 v1, v1, v68, v69
	v_max3_f32 v1, v1, v70, v71
	v_max3_f32 v1, v1, v72, v73
	v_max3_f32 v1, v1, v74, v75
	v_max3_f32 v1, v1, v76, v77
	v_mfma_f32_32x32x16_bf16 v[2:17], v[170:173], v[228:231], v[2:17]
	v_max3_f32 v1, v1, v78, v79
	v_max3_f32 v1, v1, v80, v81
	v_mov_b32_e32 v162, v1
	s_nop 1
	v_permlane32_swap_b32_e32 v1, v162
	v_max_f32_e32 v162, v162, v162
	v_max_f32_e32 v1, v1, v1
	v_max_f32_e32 v1, v1, v162
	v_max_f32_e32 v163, v217, v217
	v_max_f32_e32 v163, v163, v1
	v_sub_f32_e32 v162, v1, v217
	v_mfma_f32_32x32x16_bf16 v[2:17], v[174:177], v[236:239], v[2:17]
	v_sub_f32_e32 v1, v217, v163
	v_mul_f32_e32 v1, 0x3e0293ee, v1
	v_exp_f32_e32 v1, v1
	v_cmp_ge_f32_e32 vcc, s22, v162
	s_cmp_eq_u64 vcc, exec
	s_cselect_b64 s[2:3], -1, 0
	s_barrier
	s_waitcnt vmcnt(4)
	v_cndmask_b32_e64 v162, v1, 1.0, s[2:3]
	v_cmp_gt_f32_e32 vcc, 1.0, v162
	ds_write_b128 v203, v[146:149] offset:16384
	ds_write_b128 v204, v[150:153] offset:16384
	ds_write_b128 v201, v[154:157] offset:49152
	ds_write_b128 v202, v[158:161] offset:49152
	s_cbranch_vccz .LBB0_1151
	s_and_saveexec_b64 s[20:21], s[0:1]
	ds_write_b32 v197, v162 offset:128
	s_or_b64 exec, exec, s[20:21]
	s_waitcnt lgkmcnt(0)
	v_add_u32_e32 v1, v196, v182
	ds_read_b128 v[146:149], v1 offset:224
	ds_read_b128 v[150:153], v1 offset:192
	ds_read_b128 v[154:157], v1 offset:160
	ds_read_b128 v[158:161], v1 offset:128
	s_waitcnt lgkmcnt(3)
	v_pk_mul_f32 v[30:31], v[30:31], v[146:147]
	s_waitcnt lgkmcnt(2)
	v_pk_mul_f32 v[26:27], v[26:27], v[150:151]
	s_waitcnt lgkmcnt(1)
	v_pk_mul_f32 v[22:23], v[22:23], v[154:155]
	v_pk_mul_f32 v[32:33], v[32:33], v[148:149]
	v_pk_mul_f32 v[28:29], v[28:29], v[152:153]
	v_pk_mul_f32 v[24:25], v[24:25], v[156:157]
	s_waitcnt lgkmcnt(0)
	v_pk_mul_f32 v[20:21], v[20:21], v[160:161]
	v_pk_mul_f32 v[18:19], v[18:19], v[158:159]
	v_pk_mul_f32 v[62:63], v[62:63], v[146:147]
	v_pk_mul_f32 v[58:59], v[58:59], v[150:151]
	v_pk_mul_f32 v[54:55], v[54:55], v[154:155]
	v_pk_mul_f32 v[64:65], v[64:65], v[148:149]
	v_pk_mul_f32 v[60:61], v[60:61], v[152:153]
	v_pk_mul_f32 v[56:57], v[56:57], v[156:157]
	v_pk_mul_f32 v[52:53], v[52:53], v[160:161]
	v_pk_mul_f32 v[50:51], v[50:51], v[158:159]
	v_pk_mul_f32 v[46:47], v[46:47], v[146:147]
	v_pk_mul_f32 v[42:43], v[42:43], v[150:151]
	v_pk_mul_f32 v[38:39], v[38:39], v[154:155]
	v_pk_mul_f32 v[48:49], v[48:49], v[148:149]
	v_pk_mul_f32 v[44:45], v[44:45], v[152:153]
	v_pk_mul_f32 v[40:41], v[40:41], v[156:157]
	v_pk_mul_f32 v[36:37], v[36:37], v[160:161]
	v_pk_mul_f32 v[34:35], v[34:35], v[158:159]
	v_pk_mul_f32 v[14:15], v[14:15], v[146:147]
	v_pk_mul_f32 v[10:11], v[10:11], v[150:151]
	v_pk_mul_f32 v[6:7], v[6:7], v[154:155]
	v_pk_mul_f32 v[16:17], v[16:17], v[148:149]
	v_pk_mul_f32 v[12:13], v[12:13], v[152:153]
	v_pk_mul_f32 v[8:9], v[8:9], v[156:157]
	v_pk_mul_f32 v[4:5], v[4:5], v[160:161]
	v_pk_mul_f32 v[2:3], v[2:3], v[158:159]

.Lattn_drain0:
	s_waitcnt vmcnt(0)
	s_branch .LBB0_1147

.LBB0_1208:
	ds_read_b64_tr_b16 v[228:229], v197 offset:0
	ds_read_b64_tr_b16 v[230:231], v197 offset:0x800
	ds_read_b64_tr_b16 v[232:233], v197 offset:0x1000
	ds_read_b64_tr_b16 v[234:235], v197 offset:0x1800
	ds_read_b64_tr_b16 v[236:237], v197 offset:0x2000
	ds_read_b64_tr_b16 v[238:239], v197 offset:0x2800
	ds_read_b64_tr_b16 v[240:241], v197 offset:0x3000
	ds_read_b64_tr_b16 v[242:243], v197 offset:0x3800
	s_waitcnt lgkmcnt(0)
	s_nop 0
	v_mfma_f32_32x32x16_bf16 v[34:49], v[162:165], v[228:231], v[34:49]
	ds_read_b64_tr_b16 v[228:229], v197 offset:0x200
	ds_read_b64_tr_b16 v[230:231], v197 offset:0xa00
	v_mfma_f32_32x32x16_bf16 v[34:49], v[166:169], v[232:235], v[34:49]
	ds_read_b64_tr_b16 v[232:233], v197 offset:0x1200
	ds_read_b64_tr_b16 v[234:235], v197 offset:0x1a00
	v_mfma_f32_32x32x16_bf16 v[34:49], v[170:173], v[236:239], v[34:49]
	ds_read_b64_tr_b16 v[236:237], v197 offset:0x2200
	ds_read_b64_tr_b16 v[238:239], v197 offset:0x2a00
	ds_read_b64_tr_b16 v[244:245], v197 offset:0x3200
	ds_read_b64_tr_b16 v[246:247], v197 offset:0x3a00
	s_waitcnt lgkmcnt(0)
	v_mfma_f32_32x32x16_bf16 v[34:49], v[174:177], v[240:243], v[34:49]
	v_mfma_f32_32x32x16_bf16 v[50:65], v[162:165], v[228:231], v[50:65]
	ds_read_b64_tr_b16 v[228:229], v197 offset:0x400
	ds_read_b64_tr_b16 v[230:231], v197 offset:0xc00
	v_mfma_f32_32x32x16_bf16 v[50:65], v[166:169], v[232:235], v[50:65]
	ds_read_b64_tr_b16 v[232:233], v197 offset:0x1400
	ds_read_b64_tr_b16 v[234:235], v197 offset:0x1c00
	v_mfma_f32_32x32x16_bf16 v[50:65], v[170:173], v[236:239], v[50:65]
	ds_read_b64_tr_b16 v[236:237], v197 offset:0x2400
	ds_read_b64_tr_b16 v[238:239], v197 offset:0x2c00
	ds_read_b64_tr_b16 v[240:241], v197 offset:0x3400
	ds_read_b64_tr_b16 v[242:243], v197 offset:0x3c00
	s_waitcnt lgkmcnt(0)
	v_mfma_f32_32x32x16_bf16 v[50:65], v[174:177], v[244:247], v[50:65]
	v_mfma_f32_32x32x16_bf16 v[18:33], v[162:165], v[228:231], v[18:33]
	ds_read_b64_tr_b16 v[228:229], v197 offset:0x600
	ds_read_b64_tr_b16 v[230:231], v197 offset:0xe00
	v_mfma_f32_32x32x16_bf16 v[18:33], v[166:169], v[232:235], v[18:33]
	ds_read_b64_tr_b16 v[232:233], v197 offset:0x1600
	ds_read_b64_tr_b16 v[234:235], v197 offset:0x1e00
	v_mfma_f32_32x32x16_bf16 v[18:33], v[170:173], v[236:239], v[18:33]
	ds_read_b64_tr_b16 v[236:237], v197 offset:0x2600
	ds_read_b64_tr_b16 v[238:239], v197 offset:0x2e00
	ds_read_b64_tr_b16 v[244:245], v197 offset:0x3600
	ds_read_b64_tr_b16 v[246:247], v197 offset:0x3e00
	s_waitcnt lgkmcnt(0)
	v_mfma_f32_32x32x16_bf16 v[18:33], v[174:177], v[240:243], v[18:33]
	v_mfma_f32_32x32x16_bf16 v[2:17], v[162:165], v[228:231], v[2:17]
	v_max_f32_e32 v1, v83, v83
	v_max_f32_e32 v193, v82, v82
	v_max_f32_e32 v1, v193, v1
	v_max3_f32 v1, v1, v84, v85
	v_max3_f32 v1, v1, v86, v87
	v_max3_f32 v1, v1, v88, v89
	v_max3_f32 v1, v1, v90, v91
	v_max3_f32 v1, v1, v92, v93
	v_mfma_f32_32x32x16_bf16 v[2:17], v[166:169], v[232:235], v[2:17]
	v_max3_f32 v1, v1, v94, v95
	v_max3_f32 v1, v1, v96, v97
	v_max3_f32 v1, v1, v66, v67
	v_max3_f32 v1, v1, v68, v69
	v_max3_f32 v1, v1, v70, v71
	v_max3_f32 v1, v1, v72, v73
	v_max3_f32 v1, v1, v74, v75
	v_max3_f32 v1, v1, v76, v77
	v_mfma_f32_32x32x16_bf16 v[2:17], v[170:173], v[236:239], v[2:17]
	v_max3_f32 v1, v1, v78, v79
	v_max3_f32 v1, v1, v80, v81
	v_mov_b32_e32 v162, v1
	s_nop 1
	v_permlane32_swap_b32_e32 v1, v162
	v_max_f32_e32 v162, v162, v162
	v_max_f32_e32 v1, v1, v1
	v_max_f32_e32 v1, v1, v162
	v_max_f32_e32 v163, v225, v225
	v_max_f32_e32 v163, v163, v1
	v_sub_f32_e32 v162, v1, v225
	v_mfma_f32_32x32x16_bf16 v[2:17], v[174:177], v[244:247], v[2:17]
	v_sub_f32_e32 v1, v225, v163
	v_mul_f32_e32 v1, 0x3e0293ee, v1
	v_exp_f32_e32 v1, v1
	v_cmp_ge_f32_e32 vcc, s5, v162
	s_cmp_eq_u64 vcc, exec
	s_cselect_b64 s[2:3], -1, 0
	s_barrier
	s_waitcnt vmcnt(4)
	v_cndmask_b32_e64 v162, v1, 1.0, s[2:3]
	v_cmp_gt_f32_e32 vcc, 1.0, v162
	ds_write_b128 v202, v[146:149] offset:16384
	ds_write_b128 v203, v[150:153] offset:16384
	ds_write_b128 v204, v[154:157] offset:49152
	ds_write_b128 v205, v[158:161] offset:49152
	s_cbranch_vccz .LBB0_1212
	s_and_saveexec_b64 s[34:35], s[0:1]
	ds_write_b32 v194, v162 offset:128
	s_or_b64 exec, exec, s[34:35]
	s_waitcnt lgkmcnt(0)
	v_add_u32_e32 v1, v196, v178
	ds_read_b128 v[146:149], v1 offset:224
	ds_read_b128 v[150:153], v1 offset:192
	ds_read_b128 v[154:157], v1 offset:160
	ds_read_b128 v[158:161], v1 offset:128
	s_waitcnt lgkmcnt(3)
	v_pk_mul_f32 v[46:47], v[46:47], v[146:147]
	s_waitcnt lgkmcnt(2)
	v_pk_mul_f32 v[42:43], v[42:43], v[150:151]
	s_waitcnt lgkmcnt(1)
	v_pk_mul_f32 v[38:39], v[38:39], v[154:155]
	v_pk_mul_f32 v[48:49], v[48:49], v[148:149]
	v_pk_mul_f32 v[44:45], v[44:45], v[152:153]
	v_pk_mul_f32 v[40:41], v[40:41], v[156:157]
	s_waitcnt lgkmcnt(0)
	v_pk_mul_f32 v[36:37], v[36:37], v[160:161]
	v_pk_mul_f32 v[34:35], v[34:35], v[158:159]
	v_pk_mul_f32 v[62:63], v[62:63], v[146:147]
	v_pk_mul_f32 v[58:59], v[58:59], v[150:151]
	v_pk_mul_f32 v[54:55], v[54:55], v[154:155]
	v_pk_mul_f32 v[64:65], v[64:65], v[148:149]
	v_pk_mul_f32 v[60:61], v[60:61], v[152:153]
	v_pk_mul_f32 v[56:57], v[56:57], v[156:157]
	v_pk_mul_f32 v[52:53], v[52:53], v[160:161]
	v_pk_mul_f32 v[50:51], v[50:51], v[158:159]
	v_pk_mul_f32 v[30:31], v[30:31], v[146:147]
	v_pk_mul_f32 v[26:27], v[26:27], v[150:151]
	v_pk_mul_f32 v[22:23], v[22:23], v[154:155]
	v_pk_mul_f32 v[32:33], v[32:33], v[148:149]
	v_pk_mul_f32 v[28:29], v[28:29], v[152:153]
	v_pk_mul_f32 v[24:25], v[24:25], v[156:157]
	v_pk_mul_f32 v[20:21], v[20:21], v[160:161]
	v_pk_mul_f32 v[18:19], v[18:19], v[158:159]
	v_pk_mul_f32 v[14:15], v[14:15], v[146:147]
	v_pk_mul_f32 v[10:11], v[10:11], v[150:151]
	v_pk_mul_f32 v[6:7], v[6:7], v[154:155]
	v_pk_mul_f32 v[16:17], v[16:17], v[148:149]
	v_pk_mul_f32 v[12:13], v[12:13], v[152:153]
	v_pk_mul_f32 v[8:9], v[8:9], v[156:157]
	v_pk_mul_f32 v[4:5], v[4:5], v[160:161]
	v_pk_mul_f32 v[2:3], v[2:3], v[158:159]
